# baseline (speedup 1.0000x reference)
.LBB5_223:
	s_or_b64 exec, exec, s[0:1]
	s_movk_i32 s6, 0x290
	v_mad_u32_u24 v26, v77, s6, v74
	s_waitcnt lgkmcnt(0)
	s_barrier
	ds_read_b128 v[28:31], v26
	s_mov_b32 s8, 0xf800000
	s_movk_i32 s7, 0x140
	s_waitcnt vmcnt(2) lgkmcnt(0)
	v_pk_add_f32 v[28:29], v[22:23], v[28:29]
	v_pk_add_f32 v[30:31], v[24:25], v[30:31]
	v_add_f32_e32 v22, v28, v29
	v_add_f32_e32 v22, v22, v30
	v_add_f32_e32 v22, v22, v31
	s_nop 1
	v_mov_b32_dpp v24, v22 quad_perm:[1,0,3,2] row_mask:0xf bank_mask:0xf
	s_waitcnt lgkmcnt(0)
	v_add_f32_e32 v22, v22, v24
	s_nop 1
	v_mov_b32_dpp v25, v22 quad_perm:[2,3,0,1] row_mask:0xf bank_mask:0xf
	s_waitcnt lgkmcnt(0)
	v_add_f32_e32 v22, v22, v25
	s_nop 1
	v_mov_b32_dpp v25, v22 row_half_mirror row_mask:0xf bank_mask:0xf
	s_waitcnt lgkmcnt(0)
	v_add_f32_e32 v22, v22, v25
	s_nop 1
	v_mov_b32_dpp v25, v22 row_mirror row_mask:0xf bank_mask:0xf
	s_waitcnt lgkmcnt(0)
	v_add_f32_e32 v22, v22, v25
	v_mov_b32_e32 v25, v22
	s_nop 1
	v_permlane16_swap_b32_e32 v22, v25
	s_waitcnt lgkmcnt(0)
	v_add_f32_e32 v22, v22, v25
	v_mul_f32_e32 v22, 0x3c000000, v22
	v_pk_add_f32 v[28:29], v[28:29], v[22:23] op_sel_hi:[1,0] neg_lo:[0,1] neg_hi:[0,1]
	v_pk_add_f32 v[30:31], v[30:31], v[22:23] op_sel_hi:[1,0] neg_lo:[0,1] neg_hi:[0,1]
	v_pk_mul_f32 v[32:33], v[28:29], v[28:29]
	v_pk_mul_f32 v[34:35], v[30:31], v[30:31]
	v_add_f32_e32 v22, v32, v33
	v_add_f32_e32 v22, v34, v22
	v_add_f32_e32 v22, v35, v22
	s_nop 1
	v_mov_b32_dpp v25, v22 quad_perm:[1,0,3,2] row_mask:0xf bank_mask:0xf
	v_mov_b64_e32 v[32:33], s[4:5]
	v_mad_i64_i32 v[32:33], s[0:1], v70, s7, v[32:33]
	s_waitcnt lgkmcnt(0)
	v_add_f32_e32 v22, v22, v25
	s_nop 1
	v_mov_b32_dpp v25, v22 quad_perm:[2,3,0,1] row_mask:0xf bank_mask:0xf
	s_waitcnt lgkmcnt(0)
	v_add_f32_e32 v22, v22, v25
	s_nop 1
	v_mov_b32_dpp v25, v22 row_half_mirror row_mask:0xf bank_mask:0xf
	s_waitcnt lgkmcnt(0)
	v_add_f32_e32 v25, v22, v25
	s_nop 1
	v_mov_b32_dpp v27, v25 row_mirror row_mask:0xf bank_mask:0xf
	v_mov_b32_e32 v6, 0x3727c5ac
	v_mov_b32_e32 v22, 0x260
	s_waitcnt lgkmcnt(0)
	v_add_f32_e32 v25, v25, v27
	v_mov_b32_e32 v27, v25
	s_nop 1
	v_permlane16_swap_b32_e32 v25, v27
	v_lshlrev_b32_e32 v0, 1, v1
	v_mov_b32_e32 v1, 0
	v_lshl_add_u64 v[32:33], v[32:33], 0, v[0:1]
	s_waitcnt lgkmcnt(0)
	v_add_f32_e32 v25, v25, v27
	v_fmamk_f32 v25, v25, 0x3c000000, v6
	v_mul_f32_e32 v27, 0x4f800000, v25
	v_cmp_gt_f32_e32 vcc, s8, v25
	s_nop 1
	v_cndmask_b32_e32 v25, v25, v27, vcc
	v_sqrt_f32_e32 v27, v25
	s_nop 0
	v_add_u32_e32 v34, -1, v27
	v_add_u32_e32 v35, 1, v27
	v_fma_f32 v36, -v34, v27, v25
	v_fma_f32 v37, -v35, v27, v25
	v_cmp_ge_f32_e64 s[0:1], 0, v36
	s_nop 1
	v_cndmask_b32_e64 v27, v27, v34, s[0:1]
	v_cmp_lt_f32_e64 s[0:1], 0, v37
	s_nop 1
	v_cndmask_b32_e64 v27, v27, v35, s[0:1]
	v_mul_f32_e32 v34, 0x37800000, v27
	v_cndmask_b32_e32 v27, v27, v34, vcc
	v_cmp_class_f32_e32 vcc, v25, v22
	s_nop 1
	v_cndmask_b32_e32 v25, v27, v25, vcc
	v_div_scale_f32 v27, s[0:1], v25, v25, 1.0
	v_rcp_f32_e32 v34, v27
	v_div_scale_f32 v0, vcc, 1.0, v25, 1.0
	v_fma_f32 v35, -v27, v34, 1.0
	v_fmac_f32_e32 v34, v35, v34
	v_mul_f32_e32 v35, v0, v34
	v_fma_f32 v36, -v27, v35, v0
	v_fmac_f32_e32 v35, v36, v34
	v_fma_f32 v0, -v27, v35, v0
	v_div_fmas_f32 v0, v0, v34, v35
	v_div_fixup_f32 v0, v0, v25, 1.0
	v_pk_mul_f32 v[28:29], v[28:29], v[0:1] op_sel_hi:[1,0]
	v_pk_mul_f32 v[30:31], v[30:31], v[0:1] op_sel_hi:[1,0]
	s_waitcnt vmcnt(0)
	v_pk_fma_f32 v[10:11], v[10:11], v[28:29], v[14:15]
	v_pk_fma_f32 v[12:13], v[12:13], v[30:31], v[16:17]
	v_cvt_pk_f16_f32 v10, v10, v11
	v_cvt_pk_f16_f32 v11, v12, v13
	s_andn2_b64 vcc, exec, s[2:3]
	global_store_dwordx2 v[32:33], v[10:11], off
	s_cbranch_vccnz .LBB5_225
	v_mad_u32_u24 v0, v75, s6, v72
	ds_read_b128 v[10:13], v0 offset:512
	s_waitcnt lgkmcnt(0)
	v_pk_add_f32 v[10:11], v[18:19], v[10:11]
	v_pk_add_f32 v[12:13], v[20:21], v[12:13]
	v_add_f32_e32 v0, v10, v11
	v_add_f32_e32 v0, v0, v12
	v_add_f32_e32 v0, v0, v13
	s_nop 1
	v_mov_b32_dpp v14, v0 quad_perm:[1,0,3,2] row_mask:0xf bank_mask:0xf
	s_waitcnt lgkmcnt(0)
	v_add_f32_e32 v0, v0, v14
	s_nop 1
	v_mov_b32_dpp v14, v0 quad_perm:[2,3,0,1] row_mask:0xf bank_mask:0xf
	s_waitcnt lgkmcnt(0)
	v_add_f32_e32 v0, v0, v14
	s_nop 1
	v_mov_b32_dpp v14, v0 row_half_mirror row_mask:0xf bank_mask:0xf
	s_waitcnt lgkmcnt(0)
	v_add_f32_e32 v0, v0, v14
	v_mul_f32_e32 v0, 0x3d000000, v0
	v_pk_add_f32 v[10:11], v[10:11], v[0:1] op_sel_hi:[1,0] neg_lo:[0,1] neg_hi:[0,1]
	v_pk_add_f32 v[12:13], v[12:13], v[0:1] op_sel_hi:[1,0] neg_lo:[0,1] neg_hi:[0,1]
	v_pk_mul_f32 v[14:15], v[10:11], v[10:11]
	v_pk_mul_f32 v[16:17], v[12:13], v[12:13]
	v_add_f32_e32 v0, v14, v15
	v_add_f32_e32 v0, v16, v0
	v_add_f32_e32 v0, v17, v0
	s_nop 1
	v_mov_b32_dpp v14, v0 quad_perm:[1,0,3,2] row_mask:0xf bank_mask:0xf
	s_waitcnt lgkmcnt(0)
	v_add_f32_e32 v0, v0, v14
	s_nop 1
	v_mov_b32_dpp v14, v0 quad_perm:[2,3,0,1] row_mask:0xf bank_mask:0xf
	s_waitcnt lgkmcnt(0)
	v_add_f32_e32 v0, v0, v14
	s_nop 1
	v_mov_b32_dpp v14, v0 row_half_mirror row_mask:0xf bank_mask:0xf
	s_waitcnt lgkmcnt(0)
	v_add_f32_e32 v0, v0, v14
	v_fmac_f32_e32 v6, 0x3d000000, v0
	v_mul_f32_e32 v0, 0x4f800000, v6
	v_cmp_gt_f32_e32 vcc, s8, v6
	v_mov_b64_e32 v[14:15], s[4:5]
	s_nop 0
	v_cndmask_b32_e32 v16, v6, v0, vcc
	v_sqrt_f32_e32 v17, v16
	v_mov_b32_e32 v6, v67
	v_lshlrev_b32_e32 v0, 1, v71
	v_add_u32_e32 v18, -1, v17
	v_add_u32_e32 v19, 1, v17
	v_fma_f32 v20, -v18, v17, v16
	v_fma_f32 v21, -v19, v17, v16
	v_cmp_ge_f32_e64 s[0:1], 0, v20
	s_nop 1
	v_cndmask_b32_e64 v17, v17, v18, s[0:1]
	v_cmp_lt_f32_e64 s[0:1], 0, v21
	s_nop 1
	v_cndmask_b32_e64 v17, v17, v19, s[0:1]
	v_mul_f32_e32 v18, 0x37800000, v17
	v_cndmask_b32_e32 v17, v17, v18, vcc
	v_cmp_class_f32_e32 vcc, v16, v22
	v_mad_i64_i32 v[14:15], s[0:1], v68, s7, v[14:15]
	s_nop 0
	v_cndmask_b32_e32 v16, v17, v16, vcc
	v_div_scale_f32 v17, s[0:1], v16, v16, 1.0
	v_rcp_f32_e32 v18, v17
	v_div_scale_f32 v19, vcc, 1.0, v16, 1.0
	v_lshl_add_u64 v[0:1], v[14:15], 0, v[0:1]
	v_fma_f32 v20, -v17, v18, 1.0
	v_fmac_f32_e32 v18, v20, v18
	v_mul_f32_e32 v20, v19, v18
	v_fma_f32 v21, -v17, v20, v19
	v_fmac_f32_e32 v20, v21, v18
	v_fma_f32 v17, -v17, v20, v19
	v_div_fmas_f32 v17, v17, v18, v20
	v_div_fixup_f32 v16, v17, v16, 1.0
	v_pk_mul_f32 v[10:11], v[10:11], v[16:17] op_sel_hi:[1,0]
	v_pk_mul_f32 v[12:13], v[12:13], v[16:17] op_sel_hi:[1,0]
	v_pk_fma_f32 v[2:3], v[2:3], v[10:11], v[6:7]
	v_pk_fma_f32 v[4:5], v[4:5], v[12:13], v[8:9]
	v_cvt_pk_f16_f32 v2, v2, v3
	v_cvt_pk_f16_f32 v3, v4, v5
	global_store_dwordx2 v[0:1], v[2:3], off offset:256
